# ssd_out decayed-score blocks: 48 per-element cs/dt LDS round trips replaced by 2x8 ds_read_b128 ahead of the MFMA chains
# baseline (speedup 1.0000x reference)
.LBB0_737:
	s_or_b64 exec, exec, s[12:13]
	s_waitcnt vmcnt(0)
	v_mov_b32_e32 v2, v209
	s_waitcnt lgkmcnt(0)
	s_barrier
	ds_read_b128 v[232:235], v154
	ds_read_b128 v[236:239], v154 offset:32
	ds_read_b128 v[240:243], v154 offset:64
	ds_read_b128 v[244:247], v154 offset:96
	ds_read_b128 v[210:213], v154 offset:2048
	ds_read_b128 v[214:217], v154 offset:2080
	ds_read_b128 v[218:221], v154 offset:2112
	ds_read_b128 v[226:229], v154 offset:2144
	ds_read_b128 v[18:21], v199 offset:4096
	ds_read_b128 v[22:25], v199 offset:22528
	v_mov_b32_e32 v3, v2
	v_mov_b32_e32 v4, v2
	v_mov_b32_e32 v5, v2
	v_mov_b32_e32 v6, v2
	v_mov_b32_e32 v7, v2
	v_mov_b32_e32 v8, v2
	v_mov_b32_e32 v9, v2
	v_mov_b32_e32 v10, v2
	v_mov_b32_e32 v11, v2
	v_mov_b32_e32 v12, v2
	v_mov_b32_e32 v13, v2
	v_mov_b32_e32 v14, v2
	v_mov_b32_e32 v15, v2
	v_mov_b32_e32 v16, v2
	v_mov_b32_e32 v17, v2
	v_mov_b32_e32 v1, 0
	v_mov_b32_e32 v0, 0
	s_waitcnt lgkmcnt(0)
	v_mfma_f32_32x32x16_bf16 v[2:17], v[18:21], v[22:25], v[2:17]
	ds_read_b128 v[18:21], v199 offset:4128
	ds_read_b128 v[22:25], v199 offset:22560
	s_waitcnt lgkmcnt(0)
	v_mfma_f32_32x32x16_bf16 v[2:17], v[18:21], v[22:25], v[2:17]
	ds_read_b128 v[18:21], v199 offset:4160
	ds_read_b128 v[22:25], v199 offset:22592
	s_waitcnt lgkmcnt(0)
	v_mfma_f32_32x32x16_bf16 v[2:17], v[18:21], v[22:25], v[2:17]
	ds_read_b128 v[20:23], v199 offset:4192
	ds_read_b128 v[24:27], v199 offset:22624
	ds_read_b32 v18, v153
	s_waitcnt lgkmcnt(1)
	v_mfma_f32_32x32x16_bf16 v[2:17], v[20:23], v[24:27], v[2:17]
	s_and_saveexec_b64 vcc, s[70:71]
	s_cbranch_execz .LBB0_739
	s_waitcnt lgkmcnt(0)
	s_nop 0
	v_sub_f32_e32 v0, v18, v232
	v_mul_f32_e32 v0, 0x3fb8aa3b, v0
	v_exp_f32_e32 v0, v0
	s_nop 4
	v_mul_f32_e32 v0, v2, v0
	v_mul_f32_e32 v0, v210, v0
.LBB0_739:
	s_or_b64 exec, exec, vcc
	v_add_u32_e32 v36, 4, v154
	s_and_saveexec_b64 vcc, s[72:73]
	s_cbranch_execz .LBB0_741
	s_waitcnt lgkmcnt(0)
	s_nop 0
	v_sub_f32_e32 v1, v18, v233
	v_mul_f32_e32 v1, 0x3fb8aa3b, v1
	v_exp_f32_e32 v1, v1
	s_nop 0
	v_mul_f32_e32 v1, v3, v1
	v_mul_f32_e32 v1, v211, v1
.LBB0_741:
	s_or_b64 exec, exec, vcc
	s_nop 4
	v_mov_b32_e32 v3, 0
	v_add_u32_e32 v34, 8, v154
	v_mov_b32_e32 v2, 0
	s_mov_b64 vcc, exec
	v_readlane_b32 s12, v255, 43
	v_readlane_b32 s13, v255, 44
	s_and_b64 s[12:13], vcc, s[12:13]
	s_mov_b64 exec, s[12:13]
	s_cbranch_execz .LBB0_743
	s_waitcnt lgkmcnt(0)
	s_nop 0
	v_sub_f32_e32 v2, v18, v234
	v_mul_f32_e32 v2, 0x3fb8aa3b, v2
	v_exp_f32_e32 v2, v2
	s_nop 0
	v_mul_f32_e32 v2, v4, v2
	v_mul_f32_e32 v2, v212, v2
.LBB0_743:
	s_or_b64 exec, exec, vcc
	v_add_u32_e32 v35, 12, v154
	s_mov_b64 vcc, exec
	v_readlane_b32 s12, v255, 45
	v_readlane_b32 s13, v255, 46
	s_and_b64 s[12:13], vcc, s[12:13]
	s_mov_b64 exec, s[12:13]
	s_cbranch_execz .LBB0_745
	s_waitcnt lgkmcnt(0)
	s_nop 0
	v_sub_f32_e32 v3, v18, v235
	v_mul_f32_e32 v3, 0x3fb8aa3b, v3
	v_exp_f32_e32 v3, v3
	s_nop 0
	v_mul_f32_e32 v3, v5, v3
	v_mul_f32_e32 v3, v213, v3
.LBB0_745:
	s_or_b64 exec, exec, vcc
	v_mov_b32_e32 v5, 0
	v_add_u32_e32 v37, 32, v154
	v_mov_b32_e32 v4, 0
	s_mov_b64 vcc, exec
	v_readlane_b32 s12, v255, 47
	v_readlane_b32 s13, v255, 48
	s_and_b64 s[12:13], vcc, s[12:13]
	s_mov_b64 exec, s[12:13]
	s_cbranch_execz .LBB0_747
	s_waitcnt lgkmcnt(0)
	s_nop 0
	v_sub_f32_e32 v4, v18, v236
	v_mul_f32_e32 v4, 0x3fb8aa3b, v4
	v_exp_f32_e32 v4, v4
	s_nop 0
	v_mul_f32_e32 v4, v6, v4
	v_mul_f32_e32 v4, v214, v4
.LBB0_747:
	s_or_b64 exec, exec, vcc
	v_add_u32_e32 v38, 36, v154
	s_mov_b64 vcc, exec
	v_readlane_b32 s12, v255, 49
	v_readlane_b32 s13, v255, 50
	s_and_b64 s[12:13], vcc, s[12:13]
	s_mov_b64 exec, s[12:13]
	s_cbranch_execz .LBB0_749
	s_waitcnt lgkmcnt(0)
	s_nop 0
	v_sub_f32_e32 v5, v18, v237
	v_mul_f32_e32 v5, 0x3fb8aa3b, v5
	v_exp_f32_e32 v5, v5
	s_nop 0
	v_mul_f32_e32 v5, v7, v5
	v_mul_f32_e32 v5, v215, v5
.LBB0_749:
	s_or_b64 exec, exec, vcc
	v_mov_b32_e32 v7, 0
	v_add_u32_e32 v39, 40, v154
	v_mov_b32_e32 v6, 0
	s_mov_b64 vcc, exec
	v_readlane_b32 s12, v255, 51
	v_readlane_b32 s13, v255, 52
	s_and_b64 s[12:13], vcc, s[12:13]
	s_mov_b64 exec, s[12:13]
	s_cbranch_execz .LBB0_751
	s_waitcnt lgkmcnt(0)
	s_nop 0
	v_sub_f32_e32 v6, v18, v238
	v_mul_f32_e32 v6, 0x3fb8aa3b, v6
	v_exp_f32_e32 v6, v6
	s_nop 0
	v_mul_f32_e32 v6, v8, v6
	v_mul_f32_e32 v6, v216, v6
.LBB0_751:
	s_or_b64 exec, exec, vcc
	v_add_u32_e32 v40, 44, v154
	s_mov_b64 vcc, exec
	v_readlane_b32 s12, v255, 53
	v_readlane_b32 s13, v255, 54
	s_and_b64 s[12:13], vcc, s[12:13]
	s_mov_b64 exec, s[12:13]
	s_cbranch_execz .LBB0_753
	s_waitcnt lgkmcnt(0)
	s_nop 0
	v_sub_f32_e32 v7, v18, v239
	v_mul_f32_e32 v7, 0x3fb8aa3b, v7
	v_exp_f32_e32 v7, v7
	s_nop 0
	v_mul_f32_e32 v7, v9, v7
	v_mul_f32_e32 v7, v217, v7
.LBB0_753:
	s_or_b64 exec, exec, vcc
	v_mov_b32_e32 v9, 0
	v_add_u32_e32 v41, 64, v154
	v_mov_b32_e32 v8, 0
	s_mov_b64 vcc, exec
	v_readlane_b32 s12, v255, 55
	v_readlane_b32 s13, v255, 56
	s_and_b64 s[12:13], vcc, s[12:13]
	s_mov_b64 exec, s[12:13]
	s_cbranch_execz .LBB0_755
	s_waitcnt lgkmcnt(0)
	s_nop 0
	v_sub_f32_e32 v8, v18, v240
	v_mul_f32_e32 v8, 0x3fb8aa3b, v8
	v_exp_f32_e32 v8, v8
	s_nop 0
	v_mul_f32_e32 v8, v10, v8
	v_mul_f32_e32 v8, v218, v8
.LBB0_755:
	s_or_b64 exec, exec, vcc
	v_add_u32_e32 v42, 0x44, v154
	s_mov_b64 vcc, exec
	v_readlane_b32 s12, v255, 57
	v_readlane_b32 s13, v255, 58
	s_and_b64 s[12:13], vcc, s[12:13]
	s_mov_b64 exec, s[12:13]
	s_cbranch_execz .LBB0_757
	s_waitcnt lgkmcnt(0)
	s_nop 0
	v_sub_f32_e32 v9, v18, v241
	v_mul_f32_e32 v9, 0x3fb8aa3b, v9
	v_exp_f32_e32 v9, v9
	s_nop 0
	v_mul_f32_e32 v9, v11, v9
	v_mul_f32_e32 v9, v219, v9
.LBB0_757:
	s_or_b64 exec, exec, vcc
	v_mov_b32_e32 v11, 0
	v_add_u32_e32 v43, 0x48, v154
	v_mov_b32_e32 v10, 0
	s_mov_b64 vcc, exec
	v_readlane_b32 s12, v255, 59
	v_readlane_b32 s13, v255, 60
	s_and_b64 s[12:13], vcc, s[12:13]
	s_mov_b64 exec, s[12:13]
	s_cbranch_execz .LBB0_759
	s_waitcnt lgkmcnt(0)
	s_nop 0
	v_sub_f32_e32 v10, v18, v242
	v_mul_f32_e32 v10, 0x3fb8aa3b, v10
	v_exp_f32_e32 v10, v10
	s_nop 0
	v_mul_f32_e32 v10, v12, v10
	v_mul_f32_e32 v10, v220, v10
.LBB0_759:
	s_or_b64 exec, exec, vcc
	v_add_u32_e32 v44, 0x4c, v154
	s_mov_b64 vcc, exec
	v_readlane_b32 s12, v255, 61
	v_readlane_b32 s13, v255, 62
	s_and_b64 s[12:13], vcc, s[12:13]
	s_mov_b64 exec, s[12:13]
	s_cbranch_execz .LBB0_761
	s_waitcnt lgkmcnt(0)
	s_nop 0
	v_sub_f32_e32 v11, v18, v243
	v_mul_f32_e32 v11, 0x3fb8aa3b, v11
	v_exp_f32_e32 v11, v11
	s_nop 0
	v_mul_f32_e32 v11, v13, v11
	v_mul_f32_e32 v11, v221, v11
.LBB0_761:
	s_or_b64 exec, exec, vcc
	v_mov_b32_e32 v13, 0
	v_add_u32_e32 v45, 0x60, v154
	v_mov_b32_e32 v12, 0
	s_mov_b64 vcc, exec
	v_readlane_b32 s12, v255, 63
	v_readlane_b32 s13, v254, 0
	s_and_b64 s[12:13], vcc, s[12:13]
	s_mov_b64 exec, s[12:13]
	s_cbranch_execz .LBB0_763
	s_waitcnt lgkmcnt(0)
	s_nop 0
	v_sub_f32_e32 v12, v18, v244
	v_mul_f32_e32 v12, 0x3fb8aa3b, v12
	v_exp_f32_e32 v12, v12
	s_nop 0
	v_mul_f32_e32 v12, v14, v12
	v_mul_f32_e32 v12, v226, v12
.LBB0_763:
	s_or_b64 exec, exec, vcc
	v_add_u32_e32 v46, 0x64, v154
	s_mov_b64 vcc, exec
	v_readlane_b32 s12, v254, 1
	v_readlane_b32 s13, v254, 2
	s_and_b64 s[12:13], vcc, s[12:13]
	s_mov_b64 exec, s[12:13]
	s_cbranch_execz .LBB0_765
	s_waitcnt lgkmcnt(0)
	s_nop 0
	v_sub_f32_e32 v13, v18, v245
	v_mul_f32_e32 v13, 0x3fb8aa3b, v13
	v_exp_f32_e32 v13, v13
	s_nop 0
	v_mul_f32_e32 v13, v15, v13
	v_mul_f32_e32 v13, v227, v13
.LBB0_765:
	s_or_b64 exec, exec, vcc
	v_mov_b32_e32 v15, 0
	v_add_u32_e32 v47, 0x68, v154
	v_mov_b32_e32 v14, 0
	s_mov_b64 vcc, exec
	v_readlane_b32 s12, v254, 3
	v_readlane_b32 s13, v254, 4
	s_and_b64 s[12:13], vcc, s[12:13]
	s_mov_b64 exec, s[12:13]
	s_cbranch_execz .LBB0_767
	s_waitcnt lgkmcnt(0)
	s_nop 0
	v_sub_f32_e32 v14, v18, v246
	v_mul_f32_e32 v14, 0x3fb8aa3b, v14
	v_exp_f32_e32 v14, v14
	s_nop 0
	v_mul_f32_e32 v14, v16, v14
	v_mul_f32_e32 v14, v228, v14
.LBB0_767:
	s_or_b64 exec, exec, vcc
	v_add_u32_e32 v48, 0x6c, v154
	s_mov_b64 vcc, exec
	v_readlane_b32 s12, v254, 5
	v_readlane_b32 s13, v254, 6
	s_and_b64 s[12:13], vcc, s[12:13]
	s_mov_b64 exec, s[12:13]
	s_cbranch_execz .LBB0_769
	s_waitcnt lgkmcnt(0)
	s_nop 0
	v_sub_f32_e32 v15, v18, v247
	v_mul_f32_e32 v15, 0x3fb8aa3b, v15
	v_exp_f32_e32 v15, v15
	s_nop 0
	v_mul_f32_e32 v15, v17, v15
	v_mul_f32_e32 v15, v229, v15
.LBB0_769:
	s_or_b64 exec, exec, vcc
	s_waitcnt lgkmcnt(0)
	v_mov_b32_e32 v18, v209
	ds_read_b128 v[50:53], v199 offset:4096
	ds_read_b128 v[54:57], v200 offset:22528
	v_mov_b32_e32 v19, v18
	v_mov_b32_e32 v20, v18
	v_mov_b32_e32 v21, v18
	v_mov_b32_e32 v22, v18
	v_mov_b32_e32 v23, v18
	v_mov_b32_e32 v24, v18
	v_mov_b32_e32 v25, v18
	v_mov_b32_e32 v26, v18
	v_mov_b32_e32 v27, v18
	v_mov_b32_e32 v28, v18
	v_mov_b32_e32 v29, v18
	v_mov_b32_e32 v30, v18
	v_mov_b32_e32 v31, v18
	v_mov_b32_e32 v32, v18
	v_mov_b32_e32 v33, v18
	v_mov_b32_e32 v17, 0
	v_mov_b32_e32 v16, 0
	s_waitcnt lgkmcnt(0)
	v_mfma_f32_32x32x16_bf16 v[18:33], v[50:53], v[54:57], v[18:33]
	ds_read_b128 v[50:53], v199 offset:4128
	ds_read_b128 v[54:57], v200 offset:22560
	s_waitcnt lgkmcnt(0)
	v_mfma_f32_32x32x16_bf16 v[18:33], v[50:53], v[54:57], v[18:33]
	ds_read_b128 v[50:53], v199 offset:4160
	ds_read_b128 v[54:57], v200 offset:22592
	s_waitcnt lgkmcnt(0)
	v_mfma_f32_32x32x16_bf16 v[18:33], v[50:53], v[54:57], v[18:33]
	ds_read_b128 v[50:53], v199 offset:4192
	ds_read_b128 v[54:57], v200 offset:22624
	ds_read_b32 v49, v153 offset:128
	s_waitcnt lgkmcnt(1)
	v_mfma_f32_32x32x16_bf16 v[18:33], v[50:53], v[54:57], v[18:33]
	s_mov_b64 vcc, exec
	v_readlane_b32 s12, v254, 7
	v_readlane_b32 s13, v254, 8
	s_and_b64 s[12:13], vcc, s[12:13]
	s_mov_b64 exec, s[12:13]
	s_cbranch_execz .LBB0_771
	s_waitcnt lgkmcnt(0)
	s_nop 0
	v_sub_f32_e32 v16, v49, v232
	v_mul_f32_e32 v16, 0x3fb8aa3b, v16
	v_exp_f32_e32 v16, v16
	s_nop 0
	v_mul_f32_e32 v16, v18, v16
	v_mul_f32_e32 v16, v210, v16
.LBB0_771:
	s_or_b64 exec, exec, vcc
	s_mov_b64 vcc, exec
	v_readlane_b32 s12, v254, 9
	v_readlane_b32 s13, v254, 10
	s_and_b64 s[12:13], vcc, s[12:13]
	s_mov_b64 exec, s[12:13]
	s_cbranch_execz .LBB0_773
	s_waitcnt lgkmcnt(0)
	s_nop 0
	v_sub_f32_e32 v17, v49, v233
	v_mul_f32_e32 v17, 0x3fb8aa3b, v17
	v_exp_f32_e32 v17, v17
	s_nop 0
	v_mul_f32_e32 v17, v19, v17
	v_mul_f32_e32 v17, v211, v17
.LBB0_773:
	s_or_b64 exec, exec, vcc
	v_mov_b32_e32 v19, 0
	v_mov_b32_e32 v18, 0
	s_mov_b64 vcc, exec
	v_readlane_b32 s12, v254, 11
	v_readlane_b32 s13, v254, 12
	s_and_b64 s[12:13], vcc, s[12:13]
	s_mov_b64 exec, s[12:13]
	s_cbranch_execz .LBB0_775
	s_waitcnt lgkmcnt(0)
	s_nop 0
	v_sub_f32_e32 v18, v49, v234
	v_mul_f32_e32 v18, 0x3fb8aa3b, v18
	v_exp_f32_e32 v18, v18
	s_nop 0
	v_mul_f32_e32 v18, v20, v18
	v_mul_f32_e32 v18, v212, v18
.LBB0_775:
	s_or_b64 exec, exec, vcc
	s_mov_b64 vcc, exec
	v_readlane_b32 s12, v254, 13
	v_readlane_b32 s13, v254, 14
	s_and_b64 s[12:13], vcc, s[12:13]
	s_mov_b64 exec, s[12:13]
	s_cbranch_execz .LBB0_777
	s_waitcnt lgkmcnt(0)
	s_nop 0
	v_sub_f32_e32 v19, v49, v235
	v_mul_f32_e32 v19, 0x3fb8aa3b, v19
	v_exp_f32_e32 v19, v19
	s_nop 0
	v_mul_f32_e32 v19, v21, v19
	v_mul_f32_e32 v19, v213, v19
.LBB0_777:
	s_or_b64 exec, exec, vcc
	v_mov_b32_e32 v21, 0
	v_mov_b32_e32 v20, 0
	s_mov_b64 vcc, exec
	v_readlane_b32 s12, v254, 15
	v_readlane_b32 s13, v254, 16
	s_and_b64 s[12:13], vcc, s[12:13]
	s_mov_b64 exec, s[12:13]
	s_cbranch_execz .LBB0_779
	s_waitcnt lgkmcnt(0)
	s_nop 0
	v_sub_f32_e32 v20, v49, v236
	v_mul_f32_e32 v20, 0x3fb8aa3b, v20
	v_exp_f32_e32 v20, v20
	s_nop 0
	v_mul_f32_e32 v20, v22, v20
	v_mul_f32_e32 v20, v214, v20
.LBB0_779:
	s_or_b64 exec, exec, vcc
	s_mov_b64 vcc, exec
	v_readlane_b32 s12, v254, 17
	v_readlane_b32 s13, v254, 18
	s_and_b64 s[12:13], vcc, s[12:13]
	s_mov_b64 exec, s[12:13]
	s_cbranch_execz .LBB0_781
	s_waitcnt lgkmcnt(0)
	s_nop 0
	v_sub_f32_e32 v21, v49, v237
	v_mul_f32_e32 v21, 0x3fb8aa3b, v21
	v_exp_f32_e32 v21, v21
	s_nop 0
	v_mul_f32_e32 v21, v23, v21
	v_mul_f32_e32 v21, v215, v21
.LBB0_781:
	s_or_b64 exec, exec, vcc
	v_mov_b32_e32 v23, 0
	v_mov_b32_e32 v22, 0
	s_mov_b64 vcc, exec
	v_readlane_b32 s12, v254, 19
	v_readlane_b32 s13, v254, 20
	s_and_b64 s[12:13], vcc, s[12:13]
	s_mov_b64 exec, s[12:13]
	s_cbranch_execz .LBB0_783
	s_waitcnt lgkmcnt(0)
	s_nop 0
	v_sub_f32_e32 v22, v49, v238
	v_mul_f32_e32 v22, 0x3fb8aa3b, v22
	v_exp_f32_e32 v22, v22
	s_nop 0
	v_mul_f32_e32 v22, v24, v22
	v_mul_f32_e32 v22, v216, v22
.LBB0_783:
	s_or_b64 exec, exec, vcc
	s_and_saveexec_b64 vcc, s[22:23]
	s_cbranch_execz .LBB0_785
	s_waitcnt lgkmcnt(0)
	s_nop 0
	v_sub_f32_e32 v23, v49, v239
	v_mul_f32_e32 v23, 0x3fb8aa3b, v23
	v_exp_f32_e32 v23, v23
	s_nop 0
	v_mul_f32_e32 v23, v25, v23
	v_mul_f32_e32 v23, v217, v23
.LBB0_785:
	s_or_b64 exec, exec, vcc
	v_mov_b32_e32 v25, 0
	v_mov_b32_e32 v24, 0
	s_and_saveexec_b64 vcc, s[24:25]
	s_cbranch_execz .LBB0_787
	s_waitcnt lgkmcnt(0)
	s_nop 0
	v_sub_f32_e32 v24, v49, v240
	v_mul_f32_e32 v24, 0x3fb8aa3b, v24
	v_exp_f32_e32 v24, v24
	s_nop 0
	v_mul_f32_e32 v24, v26, v24
	v_mul_f32_e32 v24, v218, v24
.LBB0_787:
	s_or_b64 exec, exec, vcc
	s_and_saveexec_b64 vcc, s[26:27]
	s_cbranch_execz .LBB0_789
	s_waitcnt lgkmcnt(0)
	s_nop 0
	v_sub_f32_e32 v25, v49, v241
	v_mul_f32_e32 v25, 0x3fb8aa3b, v25
	v_exp_f32_e32 v25, v25
	s_nop 0
	v_mul_f32_e32 v25, v27, v25
	v_mul_f32_e32 v25, v219, v25
.LBB0_789:
	s_or_b64 exec, exec, vcc
	v_mov_b32_e32 v27, 0
	v_mov_b32_e32 v26, 0
	s_and_saveexec_b64 vcc, s[28:29]
	s_cbranch_execz .LBB0_791
	s_waitcnt lgkmcnt(0)
	s_nop 0
	v_sub_f32_e32 v26, v49, v242
	v_mul_f32_e32 v26, 0x3fb8aa3b, v26
	v_exp_f32_e32 v26, v26
	s_nop 0
	v_mul_f32_e32 v26, v28, v26
	v_mul_f32_e32 v26, v220, v26
.LBB0_791:
	s_or_b64 exec, exec, vcc
	s_and_saveexec_b64 vcc, s[30:31]
	s_cbranch_execz .LBB0_793
	s_waitcnt lgkmcnt(0)
	s_nop 0
	v_sub_f32_e32 v27, v49, v243
	v_mul_f32_e32 v27, 0x3fb8aa3b, v27
	v_exp_f32_e32 v27, v27
	s_nop 0
	v_mul_f32_e32 v27, v29, v27
	v_mul_f32_e32 v27, v221, v27
.LBB0_793:
	s_or_b64 exec, exec, vcc
	v_mov_b32_e32 v29, 0
	v_mov_b32_e32 v28, 0
	s_and_saveexec_b64 vcc, s[34:35]
	s_cbranch_execz .LBB0_795
	s_waitcnt lgkmcnt(0)
	s_nop 0
	v_sub_f32_e32 v28, v49, v244
	v_mul_f32_e32 v28, 0x3fb8aa3b, v28
	v_exp_f32_e32 v28, v28
	s_nop 0
	v_mul_f32_e32 v28, v30, v28
	v_mul_f32_e32 v28, v226, v28
.LBB0_795:
	s_or_b64 exec, exec, vcc
	s_and_saveexec_b64 vcc, s[2:3]
	s_cbranch_execz .LBB0_797
	s_waitcnt lgkmcnt(0)
	s_nop 0
	v_sub_f32_e32 v29, v49, v245
	v_mul_f32_e32 v29, 0x3fb8aa3b, v29
	v_exp_f32_e32 v29, v29
	s_nop 0
	v_mul_f32_e32 v29, v31, v29
	v_mul_f32_e32 v29, v227, v29
.LBB0_797:
	s_or_b64 exec, exec, vcc
	v_mov_b32_e32 v31, 0
	v_mov_b32_e32 v30, 0
	s_and_saveexec_b64 vcc, s[0:1]
	s_cbranch_execz .LBB0_799
	s_waitcnt lgkmcnt(0)
	s_nop 0
	v_sub_f32_e32 v30, v49, v246
	v_mul_f32_e32 v30, 0x3fb8aa3b, v30
	v_exp_f32_e32 v30, v30
	s_nop 0
	v_mul_f32_e32 v30, v32, v30
	v_mul_f32_e32 v30, v228, v30
.LBB0_799:
	s_or_b64 exec, exec, vcc
	s_and_saveexec_b64 vcc, s[36:37]
	s_cbranch_execz .LBB0_801
	s_waitcnt lgkmcnt(0)
	s_nop 0
	v_sub_f32_e32 v31, v49, v247
	v_mul_f32_e32 v31, 0x3fb8aa3b, v31
	v_exp_f32_e32 v31, v31
	s_nop 0
	v_mul_f32_e32 v31, v33, v31
	v_mul_f32_e32 v31, v229, v31
.LBB0_801:
	s_or_b64 exec, exec, vcc
	v_mov_b32_e32 v32, v209
	s_waitcnt lgkmcnt(0)
	ds_read_b128 v[232:235], v154 offset:128
	ds_read_b128 v[236:239], v154 offset:160
	ds_read_b128 v[240:243], v154 offset:192
	ds_read_b128 v[244:247], v154 offset:224
	ds_read_b128 v[210:213], v154 offset:2176
	ds_read_b128 v[214:217], v154 offset:2208
	ds_read_b128 v[218:221], v154 offset:2240
	ds_read_b128 v[226:229], v154 offset:2272
	ds_read_b128 v[48:51], v200 offset:4096
	ds_read_b128 v[52:55], v200 offset:22528
	v_mov_b32_e32 v33, v32
	v_mov_b32_e32 v34, v32
	v_mov_b32_e32 v35, v32
	v_mov_b32_e32 v36, v32
	v_mov_b32_e32 v37, v32
	v_mov_b32_e32 v38, v32
	v_mov_b32_e32 v39, v32
	v_mov_b32_e32 v40, v32
	v_mov_b32_e32 v41, v32
	v_mov_b32_e32 v42, v32
	v_mov_b32_e32 v43, v32
	v_mov_b32_e32 v44, v32
	v_mov_b32_e32 v45, v32
	v_mov_b32_e32 v46, v32
	v_mov_b32_e32 v47, v32
	s_waitcnt lgkmcnt(0)
	s_nop 0
	v_mfma_f32_32x32x16_bf16 v[32:47], v[48:51], v[52:55], v[32:47]
	ds_read_b128 v[48:51], v200 offset:4128
	ds_read_b128 v[52:55], v200 offset:22560
	s_waitcnt lgkmcnt(0)
	v_mfma_f32_32x32x16_bf16 v[32:47], v[48:51], v[52:55], v[32:47]
	ds_read_b128 v[48:51], v200 offset:4160
	ds_read_b128 v[52:55], v200 offset:22592
	s_waitcnt lgkmcnt(0)
	v_mfma_f32_32x32x16_bf16 v[32:47], v[48:51], v[52:55], v[32:47]
	ds_read_b128 v[50:53], v200 offset:4192
	ds_read_b128 v[54:57], v200 offset:22624
	ds_read_b32 v48, v153 offset:128
	v_mov_b32_e32 v49, 0
	s_waitcnt lgkmcnt(1)
	v_mfma_f32_32x32x16_bf16 v[32:47], v[50:53], v[54:57], v[32:47]
	v_mov_b32_e32 v50, 0
	s_and_saveexec_b64 vcc, s[70:71]
	s_cbranch_execz .LBB0_803
	v_add_u32_e32 v50, 0x80, v154
	s_waitcnt lgkmcnt(0)
	s_nop 0
	v_sub_f32_e32 v50, v48, v232
	v_mul_f32_e32 v50, 0x3fb8aa3b, v50
	v_exp_f32_e32 v50, v50
	s_nop 2
	v_mul_f32_e32 v32, v32, v50
	v_mul_f32_e32 v50, v210, v32
.LBB0_803:
	s_or_b64 exec, exec, vcc
	s_and_saveexec_b64 vcc, s[72:73]
	s_cbranch_execz .LBB0_805
	s_nop 5
	v_add_u32_e32 v32, 0x84, v154
	s_waitcnt lgkmcnt(0)
	s_nop 0
	v_sub_f32_e32 v32, v48, v233
	v_mul_f32_e32 v32, 0x3fb8aa3b, v32
	v_exp_f32_e32 v32, v32
	s_nop 0
	v_mul_f32_e32 v32, v33, v32
	v_mul_f32_e32 v49, v211, v32
.LBB0_805:
	s_or_b64 exec, exec, vcc
	s_nop 4
	v_mov_b32_e32 v32, 0
	v_mov_b32_e32 v33, 0
	s_and_saveexec_b64 vcc, s[38:39]
	s_cbranch_execz .LBB0_807
	v_add_u32_e32 v33, 0x88, v154
	s_waitcnt lgkmcnt(0)
	s_nop 0
	v_sub_f32_e32 v33, v48, v234
	v_mul_f32_e32 v33, 0x3fb8aa3b, v33
	v_exp_f32_e32 v33, v33
	s_nop 0
	v_mul_f32_e32 v33, v34, v33
	v_mul_f32_e32 v33, v212, v33
.LBB0_807:
	s_or_b64 exec, exec, vcc
	s_and_saveexec_b64 vcc, s[40:41]
	s_cbranch_execz .LBB0_809
	v_add_u32_e32 v32, 0x8c, v154
	s_waitcnt lgkmcnt(0)
	s_nop 0
	v_sub_f32_e32 v32, v48, v235
	v_mul_f32_e32 v32, 0x3fb8aa3b, v32
	v_exp_f32_e32 v32, v32
	s_nop 0
	v_mul_f32_e32 v32, v35, v32
	v_mul_f32_e32 v32, v213, v32
.LBB0_809:
	s_or_b64 exec, exec, vcc
	v_mov_b32_e32 v34, 0
	v_mov_b32_e32 v35, 0
	s_and_saveexec_b64 vcc, s[42:43]
	s_cbranch_execz .LBB0_811
	v_add_u32_e32 v35, 0xa0, v154
	s_waitcnt lgkmcnt(0)
	s_nop 0
	v_sub_f32_e32 v35, v48, v236
	v_mul_f32_e32 v35, 0x3fb8aa3b, v35
	v_exp_f32_e32 v35, v35
	s_nop 0
	v_mul_f32_e32 v35, v36, v35
	v_mul_f32_e32 v35, v214, v35
.LBB0_811:
	s_or_b64 exec, exec, vcc
	s_and_saveexec_b64 vcc, s[44:45]
	s_cbranch_execz .LBB0_813
	v_add_u32_e32 v34, 0xa4, v154
	s_waitcnt lgkmcnt(0)
	s_nop 0
	v_sub_f32_e32 v34, v48, v237
	v_mul_f32_e32 v34, 0x3fb8aa3b, v34
	v_exp_f32_e32 v34, v34
	s_nop 0
	v_mul_f32_e32 v34, v37, v34
	v_mul_f32_e32 v34, v215, v34
.LBB0_813:
	s_or_b64 exec, exec, vcc
	v_mov_b32_e32 v36, 0
	v_mov_b32_e32 v37, 0
	s_and_saveexec_b64 vcc, s[46:47]
	s_cbranch_execz .LBB0_815
	v_add_u32_e32 v37, 0xa8, v154
	s_waitcnt lgkmcnt(0)
	s_nop 0
	v_sub_f32_e32 v37, v48, v238
	v_mul_f32_e32 v37, 0x3fb8aa3b, v37
	v_exp_f32_e32 v37, v37
	s_nop 0
	v_mul_f32_e32 v37, v38, v37
	v_mul_f32_e32 v37, v216, v37
.LBB0_815:
	s_or_b64 exec, exec, vcc
	s_and_saveexec_b64 vcc, s[48:49]
	s_cbranch_execz .LBB0_817
	v_add_u32_e32 v36, 0xac, v154
	s_waitcnt lgkmcnt(0)
	s_nop 0
	v_sub_f32_e32 v36, v48, v239
	v_mul_f32_e32 v36, 0x3fb8aa3b, v36
	v_exp_f32_e32 v36, v36
	s_nop 0
	v_mul_f32_e32 v36, v39, v36
	v_mul_f32_e32 v36, v217, v36
.LBB0_817:
	s_or_b64 exec, exec, vcc
	v_mov_b32_e32 v38, 0
	v_mov_b32_e32 v39, 0
	s_and_saveexec_b64 vcc, s[50:51]
	s_cbranch_execz .LBB0_819
	v_add_u32_e32 v39, 0xc0, v154
	s_waitcnt lgkmcnt(0)
	s_nop 0
	v_sub_f32_e32 v39, v48, v240
	v_mul_f32_e32 v39, 0x3fb8aa3b, v39
	v_exp_f32_e32 v39, v39
	s_nop 0
	v_mul_f32_e32 v39, v40, v39
	v_mul_f32_e32 v39, v218, v39
.LBB0_819:
	s_or_b64 exec, exec, vcc
	s_and_saveexec_b64 vcc, s[52:53]
	s_cbranch_execz .LBB0_821
	v_add_u32_e32 v38, 0xc4, v154
	s_waitcnt lgkmcnt(0)
	s_nop 0
	v_sub_f32_e32 v38, v48, v241
	v_mul_f32_e32 v38, 0x3fb8aa3b, v38
	v_exp_f32_e32 v38, v38
	s_nop 0
	v_mul_f32_e32 v38, v41, v38
	v_mul_f32_e32 v38, v219, v38
.LBB0_821:
	s_or_b64 exec, exec, vcc
	v_mov_b32_e32 v40, 0
	v_mov_b32_e32 v41, 0
	s_and_saveexec_b64 vcc, s[54:55]
	s_cbranch_execz .LBB0_823
	v_add_u32_e32 v41, 0xc8, v154
	s_waitcnt lgkmcnt(0)
	s_nop 0
	v_sub_f32_e32 v41, v48, v242
	v_mul_f32_e32 v41, 0x3fb8aa3b, v41
	v_exp_f32_e32 v41, v41
	s_nop 0
	v_mul_f32_e32 v41, v42, v41
	v_mul_f32_e32 v41, v220, v41
.LBB0_823:
	s_or_b64 exec, exec, vcc
	s_and_saveexec_b64 vcc, s[56:57]
	s_cbranch_execz .LBB0_825
	v_add_u32_e32 v40, 0xcc, v154
	s_waitcnt lgkmcnt(0)
	s_nop 0
	v_sub_f32_e32 v40, v48, v243
	v_mul_f32_e32 v40, 0x3fb8aa3b, v40
	v_exp_f32_e32 v40, v40
	s_nop 0
	v_mul_f32_e32 v40, v43, v40
	v_mul_f32_e32 v40, v221, v40
.LBB0_825:
	s_or_b64 exec, exec, vcc
	v_mov_b32_e32 v42, 0
	v_mov_b32_e32 v43, 0
	s_and_saveexec_b64 vcc, s[58:59]
	s_cbranch_execz .LBB0_827
	v_add_u32_e32 v43, 0xe0, v154
	s_waitcnt lgkmcnt(0)
	s_nop 0
	v_sub_f32_e32 v43, v48, v244
	v_mul_f32_e32 v43, 0x3fb8aa3b, v43
	v_exp_f32_e32 v43, v43
	s_nop 0
	v_mul_f32_e32 v43, v44, v43
	v_mul_f32_e32 v43, v226, v43
.LBB0_827:
	s_or_b64 exec, exec, vcc
	s_and_saveexec_b64 vcc, s[60:61]
	s_cbranch_execz .LBB0_829
	v_add_u32_e32 v42, 0xe4, v154
	s_waitcnt lgkmcnt(0)
	s_nop 0
	v_sub_f32_e32 v42, v48, v245
	v_mul_f32_e32 v42, 0x3fb8aa3b, v42
	v_exp_f32_e32 v42, v42
	s_nop 0
	v_mul_f32_e32 v42, v45, v42
	v_mul_f32_e32 v42, v227, v42
.LBB0_829:
	s_or_b64 exec, exec, vcc
	v_mov_b32_e32 v44, 0
	v_mov_b32_e32 v45, 0
	s_and_saveexec_b64 vcc, s[14:15]
	s_cbranch_execz .LBB0_831
	v_add_u32_e32 v45, 0xe8, v154
	s_waitcnt lgkmcnt(0)
	s_nop 0
	v_sub_f32_e32 v45, v48, v246
	v_mul_f32_e32 v45, 0x3fb8aa3b, v45
	v_exp_f32_e32 v45, v45
	s_nop 0
	v_mul_f32_e32 v45, v46, v45
	v_mul_f32_e32 v45, v228, v45
.LBB0_831:
	s_or_b64 exec, exec, vcc
	s_and_saveexec_b64 vcc, s[16:17]
	s_cbranch_execz .LBB0_833
	v_add_u32_e32 v44, 0xec, v154
	s_waitcnt lgkmcnt(0)
	s_nop 0
	v_sub_f32_e32 v44, v48, v247
	v_mul_f32_e32 v44, 0x3fb8aa3b, v44
	v_exp_f32_e32 v44, v44
	s_nop 0
	v_mul_f32_e32 v44, v47, v44
	v_mul_f32_e32 v44, v229, v44
